# v041 + the first workgroup of each XCD to arrive at a grid barrier starts the L2 write-back early (buffer_wbl2), so the XCD leader's write-back before the global arrival is short
# baseline (speedup 1.0000x reference)
.LBB0_180:
	s_or_b64 exec, exec, s[4:5]
	v_cvt_f32_u32_e32 v6, v3
	s_waitcnt vmcnt(0)
	v_readfirstlane_b32 s4, v5
	v_sub_u32_e32 v5, 0, v3
	v_rcp_iflag_f32_e32 v6, v6
	v_add_u32_e32 v7, s4, v4
	v_mul_f32_e32 v6, 0x4f7ffffe, v6
	v_cvt_u32_f32_e32 v6, v6
	v_mul_lo_u32 v4, v5, v6
	v_mul_hi_u32 v4, v6, v4
	v_add_u32_e32 v4, v6, v4
	v_mul_hi_u32 v4, v7, v4
	v_mul_lo_u32 v5, v4, v3
	v_sub_u32_e32 v5, v7, v5
	v_add_u32_e32 v6, 1, v4
	v_cmp_ge_u32_e32 vcc, v5, v3
	s_nop 1
	v_cndmask_b32_e32 v4, v4, v6, vcc
	v_sub_u32_e32 v6, v5, v3
	v_cndmask_b32_e32 v5, v5, v6, vcc
	v_add_u32_e32 v6, 1, v4
	v_cmp_ge_u32_e32 vcc, v5, v3
	v_add_u32_e32 v5, 1, v7
	s_nop 0
	v_cndmask_b32_e32 v4, v4, v6, vcc
	v_mul_lo_u32 v6, v3, v4
	v_add_u32_e32 v3, v6, v3
	v_cmp_ne_u32_e32 vcc, v5, v3
	s_and_saveexec_b64 s[4:5], vcc
	s_xor_b64 s[4:5], exec, s[4:5]
	s_cbranch_execz .LBB0_194
	v_cmp_eq_u32_e32 vcc, v7, v6
	s_cbranch_vccz .Lfw_0
	buffer_wbl2 sc1
.Lfw_0:
	v_mad_u32_u24 v6, v4, v2, v2
	v_readlane_b32 s6, v254, 18
	v_readlane_b32 s7, v254, 19
	s_waitcnt lgkmcnt(0)
	s_nop 3
	global_load_dword v2, v207, s[6:7] sc1
	s_waitcnt vmcnt(0)
	v_cmp_lt_u32_e32 vcc, v2, v6
	s_and_saveexec_b64 s[6:7], vcc
	s_cbranch_execz .LBB0_193
	s_mov_b32 s23, 1
	s_mov_b64 s[8:9], 0
	s_branch .LBB0_184

.Lfw_1:
	v_mad_u32_u24 v6, v4, v2, v2
	v_readlane_b32 s6, v254, 18
	v_readlane_b32 s7, v254, 19
	s_waitcnt lgkmcnt(0)
	s_nop 3
	global_load_dword v2, v207, s[6:7] sc1
	s_waitcnt vmcnt(0)
	v_cmp_lt_u32_e32 vcc, v2, v6
	s_and_saveexec_b64 s[6:7], vcc
	s_cbranch_execz .LBB0_309
	s_mov_b32 s10, 1
	s_mov_b64 s[8:9], 0
	s_branch .LBB0_300
